# expert gate/up GEMM epilogue hand-scheduled stage-major (8 outputs per store, no pair shuffles or s_nop pads, same f32 ops) + combine layer-0 norm loads hoisted
# speedup vs baseline: 1.0068x; 1.0068x over previous
; __device__ __forceinline__ float sigmoid_(float x) { return 1.f / (1.f + __expf(-x)); }
; __device__ __forceinline__ float silu_(float x) { return x * sigmoid_(x); }
; __device__ __forceinline__ float sigmoid_fast(float x) { return __builtin_amdgcn_rcpf(1.f + __expf(-x)); }
; __device__ __forceinline__ float silu_fast(float x) { return x * sigmoid_fast(x); }
; __device__ __forceinline__ float one_minus_exp(float x) { const float p = -x * (1.f + x * (0.5f + x * (0.16666667f + x * (0.041666668f + x * 0.0083333338f)))); return x > -0.1f ? p : 1.f - __expf(x); }
; __device__ __forceinline__ float sat8(float x) { return __builtin_amdgcn_fmed3f(x, -448.f, 448.f); }
; __device__ __forceinline__ unsigned pk4_fp8(float a, float b, float c, float d) { int w = __builtin_amdgcn_cvt_pk_fp8_f32(sat8(a), sat8(b), 0, false); w = __builtin_amdgcn_cvt_pk_fp8_f32(sat8(c), sat8(d), w, true); return (unsigned)w; }
;     __device__ __forceinline__ void epi(const f32x4 (&acc)[2][2][4][2], const Unit& u, int wr, int wc, int fr, int fq) const {
;         const int e = u.pm / tpe, t = u.pm - e * tpe;
;         char* base = (char*)(ACT + ((size_t)e * EROWS + (size_t)t * 256) * 2048 + (size_t)u.pn * 128);
;         unsigned loff = (unsigned)((wr * 64 + fr) * 2048 + wc * 32 + 8 * fq); asm volatile("" : "+v"(loff));
;         constexpr float S = 1.f / W8_SCALE;
; #pragma unroll
;         for (int ai = 0; ai < 2; ++ai)
; #pragma unroll
;             for (int m = 0; m < 4; ++m) {
;                 float o[8];
; #pragma unroll
;                 for (int n = 0; n < 2; ++n)
; #pragma unroll
;                     for (int j = 0; j < 4; ++j) o[n * 4 + j] = silu_fast(acc[ai][0][m][n][j] * S) * (acc[ai][1][m][n][j] * S);
;                 u32x2 w; w.x = pk4_fp8(o[0], o[1], o[2], o[3]); w.y = pk4_fp8(o[4], o[5], o[6], o[7]);
;                 *(u32x2*)(base + (size_t)(ai * 128 + m * 16) * 2048 + loff) = w; }
.LBB0_2590:
	s_abs_i32 s18, s17
	s_mul_hi_u32 s19, s18, s47
	s_mul_i32 s20, s19, s24
	s_sub_i32 s18, s18, s20
	s_ashr_i32 s11, s17, 31
	s_add_i32 s20, s19, 1
	s_sub_i32 s21, s18, s24
	s_cmp_ge_u32 s18, s24
	s_cselect_b32 s19, s20, s19
	s_cselect_b32 s18, s21, s18
	s_add_i32 s20, s19, 1
	s_cmp_ge_u32 s18, s24
	s_cselect_b32 s18, s20, s19
	s_xor_b32 s18, s18, s11
	s_sub_i32 s11, s18, s11
	s_mul_i32 s18, s11, s24
	s_sub_i32 s18, s17, s18
	s_ashr_i32 s19, s18, 31
	s_lshl_b64 s[18:19], s[18:19], 19
	s_add_u32 s18, s52, s18
	s_mul_hi_i32 s17, s11, 0x480000
	s_mul_i32 s11, s11, 0x480000
	s_addc_u32 s19, s53, s19
	s_add_u32 s11, s18, s11
	s_addc_u32 s18, s19, s17
	s_ashr_i32 s17, s16, 31
	s_lshl_b64 s[16:17], s[16:17], 7
	s_add_u32 s16, s11, s16
	s_addc_u32 s17, s18, s17
	v_mov_b32_e32 v146, v187
	v_mul_f32_e32 v156, 0x3c800000, v156
	v_mul_f32_e32 v157, 0x3c800000, v157
	v_mul_f32_e32 v158, 0x3c800000, v158
	v_mul_f32_e32 v159, 0x3c800000, v159
	v_mul_f32_e32 v148, 0x3c800000, v148
	v_mul_f32_e32 v149, 0x3c800000, v149
	v_mul_f32_e32 v150, 0x3c800000, v150
	v_mul_f32_e32 v151, 0x3c800000, v151
	v_mul_f32_e32 v4, 0xbfb8aa3b, v156
	v_mul_f32_e32 v5, 0xbfb8aa3b, v157
	v_mul_f32_e32 v6, 0xbfb8aa3b, v158
	v_mul_f32_e32 v7, 0xbfb8aa3b, v159
	v_mul_f32_e32 v8, 0xbfb8aa3b, v148
	v_mul_f32_e32 v9, 0xbfb8aa3b, v149
	v_mul_f32_e32 v10, 0xbfb8aa3b, v150
	v_mul_f32_e32 v11, 0xbfb8aa3b, v151
	v_exp_f32_e32 v4, v4
	v_exp_f32_e32 v5, v5
	v_exp_f32_e32 v6, v6
	v_exp_f32_e32 v7, v7
	v_exp_f32_e32 v8, v8
	v_exp_f32_e32 v9, v9
	v_exp_f32_e32 v10, v10
	v_exp_f32_e32 v11, v11
	v_mul_f32_e32 v160, 0x3c800000, v160
	v_mul_f32_e32 v161, 0x3c800000, v161
	v_mul_f32_e32 v162, 0x3c800000, v162
	v_mul_f32_e32 v163, 0x3c800000, v163
	v_mul_f32_e32 v152, 0x3c800000, v152
	v_mul_f32_e32 v153, 0x3c800000, v153
	v_mul_f32_e32 v154, 0x3c800000, v154
	v_mul_f32_e32 v155, 0x3c800000, v155
	v_add_f32_e32 v4, 1.0, v4
	v_add_f32_e32 v5, 1.0, v5
	v_add_f32_e32 v6, 1.0, v6
	v_add_f32_e32 v7, 1.0, v7
	v_add_f32_e32 v8, 1.0, v8
	v_add_f32_e32 v9, 1.0, v9
	v_add_f32_e32 v10, 1.0, v10
	v_add_f32_e32 v11, 1.0, v11
	v_rcp_f32_e32 v4, v4
	v_rcp_f32_e32 v5, v5
	v_rcp_f32_e32 v6, v6
	v_rcp_f32_e32 v7, v7
	v_rcp_f32_e32 v8, v8
	v_rcp_f32_e32 v9, v9
	v_rcp_f32_e32 v10, v10
	v_rcp_f32_e32 v11, v11
	v_mov_b32_e32 v16, v146
	v_mov_b32_e32 v12, v147
	v_mov_b32_e32 v13, v147
	v_mul_f32_e32 v4, v156, v4
	v_mul_f32_e32 v5, v157, v5
	v_mul_f32_e32 v6, v158, v6
	v_mul_f32_e32 v7, v159, v7
	v_mul_f32_e32 v8, v148, v8
	v_mul_f32_e32 v9, v149, v9
	v_mul_f32_e32 v10, v150, v10
	v_mul_f32_e32 v11, v151, v11
	v_mul_f32_e32 v4, v160, v4
	v_mul_f32_e32 v5, v161, v5
	v_mul_f32_e32 v6, v162, v6
	v_mul_f32_e32 v7, v163, v7
	v_mul_f32_e32 v8, v152, v8
	v_mul_f32_e32 v9, v153, v9
	v_mul_f32_e32 v10, v154, v10
	v_mul_f32_e32 v11, v155, v11
	v_med3_f32 v4, v4, s30, v224
	v_med3_f32 v5, v5, s30, v224
	v_med3_f32 v6, v6, s30, v224
	v_med3_f32 v7, v7, s30, v224
	v_med3_f32 v8, v8, s30, v224
	v_med3_f32 v9, v9, s30, v224
	v_med3_f32 v10, v10, s30, v224
	v_med3_f32 v11, v11, s30, v224
	v_cvt_pk_fp8_f32 v12, v4, v5
	v_cvt_pk_fp8_f32 v12, v6, v7 op_sel:[0,0,1]
	v_cvt_pk_fp8_f32 v13, v8, v9
	v_cvt_pk_fp8_f32 v13, v10, v11 op_sel:[0,0,1]
	global_store_dwordx2 v16, v[12:13], s[16:17]
	v_mul_f32_e32 v138, 0x3c800000, v138
	v_mul_f32_e32 v139, 0x3c800000, v139
	v_mul_f32_e32 v140, 0x3c800000, v140
	v_mul_f32_e32 v141, 0x3c800000, v141
	v_mul_f32_e32 v130, 0x3c800000, v130
	v_mul_f32_e32 v131, 0x3c800000, v131
	v_mul_f32_e32 v132, 0x3c800000, v132
	v_mul_f32_e32 v133, 0x3c800000, v133
	v_mul_f32_e32 v4, 0xbfb8aa3b, v138
	v_mul_f32_e32 v5, 0xbfb8aa3b, v139
	v_mul_f32_e32 v6, 0xbfb8aa3b, v140
	v_mul_f32_e32 v7, 0xbfb8aa3b, v141
	v_mul_f32_e32 v8, 0xbfb8aa3b, v130
	v_mul_f32_e32 v9, 0xbfb8aa3b, v131
	v_mul_f32_e32 v10, 0xbfb8aa3b, v132
	v_mul_f32_e32 v11, 0xbfb8aa3b, v133
	v_exp_f32_e32 v4, v4
	v_exp_f32_e32 v5, v5
	v_exp_f32_e32 v6, v6
	v_exp_f32_e32 v7, v7
	v_exp_f32_e32 v8, v8
	v_exp_f32_e32 v9, v9
	v_exp_f32_e32 v10, v10
	v_exp_f32_e32 v11, v11
	v_mul_f32_e32 v142, 0x3c800000, v142
	v_mul_f32_e32 v143, 0x3c800000, v143
	v_mul_f32_e32 v144, 0x3c800000, v144
	v_mul_f32_e32 v145, 0x3c800000, v145
	v_mul_f32_e32 v134, 0x3c800000, v134
	v_mul_f32_e32 v135, 0x3c800000, v135
	v_mul_f32_e32 v136, 0x3c800000, v136
	v_mul_f32_e32 v137, 0x3c800000, v137
	v_add_f32_e32 v4, 1.0, v4
	v_add_f32_e32 v5, 1.0, v5
	v_add_f32_e32 v6, 1.0, v6
	v_add_f32_e32 v7, 1.0, v7
	v_add_f32_e32 v8, 1.0, v8
	v_add_f32_e32 v9, 1.0, v9
	v_add_f32_e32 v10, 1.0, v10
	v_add_f32_e32 v11, 1.0, v11
	v_rcp_f32_e32 v4, v4
	v_rcp_f32_e32 v5, v5
	v_rcp_f32_e32 v6, v6
	v_rcp_f32_e32 v7, v7
	v_rcp_f32_e32 v8, v8
	v_rcp_f32_e32 v9, v9
	v_rcp_f32_e32 v10, v10
	v_rcp_f32_e32 v11, v11
	v_add_u32_e32 v17, 0x8000, v146
	v_mov_b32_e32 v14, v147
	v_mov_b32_e32 v15, v147
	v_mul_f32_e32 v4, v138, v4
	v_mul_f32_e32 v5, v139, v5
	v_mul_f32_e32 v6, v140, v6
	v_mul_f32_e32 v7, v141, v7
	v_mul_f32_e32 v8, v130, v8
	v_mul_f32_e32 v9, v131, v9
	v_mul_f32_e32 v10, v132, v10
	v_mul_f32_e32 v11, v133, v11
	v_mul_f32_e32 v4, v142, v4
	v_mul_f32_e32 v5, v143, v5
	v_mul_f32_e32 v6, v144, v6
	v_mul_f32_e32 v7, v145, v7
	v_mul_f32_e32 v8, v134, v8
	v_mul_f32_e32 v9, v135, v9
	v_mul_f32_e32 v10, v136, v10
	v_mul_f32_e32 v11, v137, v11
	v_med3_f32 v4, v4, s30, v224
	v_med3_f32 v5, v5, s30, v224
	v_med3_f32 v6, v6, s30, v224
	v_med3_f32 v7, v7, s30, v224
	v_med3_f32 v8, v8, s30, v224
	v_med3_f32 v9, v9, s30, v224
	v_med3_f32 v10, v10, s30, v224
	v_med3_f32 v11, v11, s30, v224
	v_cvt_pk_fp8_f32 v14, v4, v5
	v_cvt_pk_fp8_f32 v14, v6, v7 op_sel:[0,0,1]
	v_cvt_pk_fp8_f32 v15, v8, v9
; __device__ __forceinline__ float sigmoid_(float x) { return 1.f / (1.f + __expf(-x)); }
; __device__ __forceinline__ float silu_(float x) { return x * sigmoid_(x); }
; __device__ __forceinline__ float sigmoid_fast(float x) { return __builtin_amdgcn_rcpf(1.f + __expf(-x)); }
; __device__ __forceinline__ float silu_fast(float x) { return x * sigmoid_fast(x); }
; __device__ __forceinline__ float one_minus_exp(float x) { const float p = -x * (1.f + x * (0.5f + x * (0.16666667f + x * (0.041666668f + x * 0.0083333338f)))); return x > -0.1f ? p : 1.f - __expf(x); }
; __device__ __forceinline__ float sat8(float x) { return __builtin_amdgcn_fmed3f(x, -448.f, 448.f); }
; __device__ __forceinline__ unsigned pk4_fp8(float a, float b, float c, float d) { int w = __builtin_amdgcn_cvt_pk_fp8_f32(sat8(a), sat8(b), 0, false); w = __builtin_amdgcn_cvt_pk_fp8_f32(sat8(c), sat8(d), w, true); return (unsigned)w; }
;     __device__ __forceinline__ void epi(const f32x4 (&acc)[2][2][4][2], const Unit& u, int wr, int wc, int fr, int fq) const {
;     ...
; #pragma unroll
;         for (int ai = 0; ai < 2; ++ai)
; #pragma unroll
;             for (int m = 0; m < 4; ++m) {
;                 float o[8];
; #pragma unroll
;                 for (int n = 0; n < 2; ++n)
; #pragma unroll
;                     for (int j = 0; j < 4; ++j) o[n * 4 + j] = silu_fast(acc[ai][0][m][n][j] * S) * (acc[ai][1][m][n][j] * S);
;                 u32x2 w; w.x = pk4_fp8(o[0], o[1], o[2], o[3]); w.y = pk4_fp8(o[4], o[5], o[6], o[7]);
;                 *(u32x2*)(base + (size_t)(ai * 128 + m * 16) * 2048 + loff) = w; }
	v_cvt_pk_fp8_f32 v15, v10, v11 op_sel:[0,0,1]
	global_store_dwordx2 v17, v[14:15], s[16:17]
	v_mul_f32_e32 v122, 0x3c800000, v122
	v_mul_f32_e32 v123, 0x3c800000, v123
	v_mul_f32_e32 v124, 0x3c800000, v124
	v_mul_f32_e32 v125, 0x3c800000, v125
	v_mul_f32_e32 v114, 0x3c800000, v114
	v_mul_f32_e32 v115, 0x3c800000, v115
	v_mul_f32_e32 v116, 0x3c800000, v116
	v_mul_f32_e32 v117, 0x3c800000, v117
	v_mul_f32_e32 v4, 0xbfb8aa3b, v122
	v_mul_f32_e32 v5, 0xbfb8aa3b, v123
	v_mul_f32_e32 v6, 0xbfb8aa3b, v124
	v_mul_f32_e32 v7, 0xbfb8aa3b, v125
	v_mul_f32_e32 v8, 0xbfb8aa3b, v114
	v_mul_f32_e32 v9, 0xbfb8aa3b, v115
	v_mul_f32_e32 v10, 0xbfb8aa3b, v116
	v_mul_f32_e32 v11, 0xbfb8aa3b, v117
	v_exp_f32_e32 v4, v4
	v_exp_f32_e32 v5, v5
	v_exp_f32_e32 v6, v6
	v_exp_f32_e32 v7, v7
	v_exp_f32_e32 v8, v8
	v_exp_f32_e32 v9, v9
	v_exp_f32_e32 v10, v10
	v_exp_f32_e32 v11, v11
	v_mul_f32_e32 v126, 0x3c800000, v126
	v_mul_f32_e32 v127, 0x3c800000, v127
	v_mul_f32_e32 v128, 0x3c800000, v128
	v_mul_f32_e32 v129, 0x3c800000, v129
	v_mul_f32_e32 v118, 0x3c800000, v118
	v_mul_f32_e32 v119, 0x3c800000, v119
	v_mul_f32_e32 v120, 0x3c800000, v120
	v_mul_f32_e32 v121, 0x3c800000, v121
	v_add_f32_e32 v4, 1.0, v4
	v_add_f32_e32 v5, 1.0, v5
	v_add_f32_e32 v6, 1.0, v6
	v_add_f32_e32 v7, 1.0, v7
	v_add_f32_e32 v8, 1.0, v8
	v_add_f32_e32 v9, 1.0, v9
	v_add_f32_e32 v10, 1.0, v10
	v_add_f32_e32 v11, 1.0, v11
	v_rcp_f32_e32 v4, v4
	v_rcp_f32_e32 v5, v5
	v_rcp_f32_e32 v6, v6
	v_rcp_f32_e32 v7, v7
	v_rcp_f32_e32 v8, v8
	v_rcp_f32_e32 v9, v9
	v_rcp_f32_e32 v10, v10
	v_rcp_f32_e32 v11, v11
	v_add_u32_e32 v16, 0x10000, v146
	v_mov_b32_e32 v12, v147
	v_mov_b32_e32 v13, v147
	v_mul_f32_e32 v4, v122, v4
	v_mul_f32_e32 v5, v123, v5
	v_mul_f32_e32 v6, v124, v6
	v_mul_f32_e32 v7, v125, v7
	v_mul_f32_e32 v8, v114, v8
	v_mul_f32_e32 v9, v115, v9
	v_mul_f32_e32 v10, v116, v10
	v_mul_f32_e32 v11, v117, v11
	v_mul_f32_e32 v4, v126, v4
	v_mul_f32_e32 v5, v127, v5
	v_mul_f32_e32 v6, v128, v6
	v_mul_f32_e32 v7, v129, v7
	v_mul_f32_e32 v8, v118, v8
	v_mul_f32_e32 v9, v119, v9
	v_mul_f32_e32 v10, v120, v10
	v_mul_f32_e32 v11, v121, v11
	v_med3_f32 v4, v4, s30, v224
	v_med3_f32 v5, v5, s30, v224
	v_med3_f32 v6, v6, s30, v224
	v_med3_f32 v7, v7, s30, v224
	v_med3_f32 v8, v8, s30, v224
	v_med3_f32 v9, v9, s30, v224
	v_med3_f32 v10, v10, s30, v224
	v_med3_f32 v11, v11, s30, v224
	v_cvt_pk_fp8_f32 v12, v4, v5
	v_cvt_pk_fp8_f32 v12, v6, v7 op_sel:[0,0,1]
	v_cvt_pk_fp8_f32 v13, v8, v9
	v_cvt_pk_fp8_f32 v13, v10, v11 op_sel:[0,0,1]
	global_store_dwordx2 v16, v[12:13], s[16:17]
	v_mul_f32_e32 v106, 0x3c800000, v106
	v_mul_f32_e32 v107, 0x3c800000, v107
	v_mul_f32_e32 v108, 0x3c800000, v108
	v_mul_f32_e32 v109, 0x3c800000, v109
	v_mul_f32_e32 v98, 0x3c800000, v98
	v_mul_f32_e32 v99, 0x3c800000, v99
	v_mul_f32_e32 v100, 0x3c800000, v100
	v_mul_f32_e32 v101, 0x3c800000, v101
	v_mul_f32_e32 v4, 0xbfb8aa3b, v106
	v_mul_f32_e32 v5, 0xbfb8aa3b, v107
	v_mul_f32_e32 v6, 0xbfb8aa3b, v108
	v_mul_f32_e32 v7, 0xbfb8aa3b, v109
	v_mul_f32_e32 v8, 0xbfb8aa3b, v98
	v_mul_f32_e32 v9, 0xbfb8aa3b, v99
	v_mul_f32_e32 v10, 0xbfb8aa3b, v100
	v_mul_f32_e32 v11, 0xbfb8aa3b, v101
	v_exp_f32_e32 v4, v4
	v_exp_f32_e32 v5, v5
	v_exp_f32_e32 v6, v6
	v_exp_f32_e32 v7, v7
	v_exp_f32_e32 v8, v8
	v_exp_f32_e32 v9, v9
	v_exp_f32_e32 v10, v10
	v_exp_f32_e32 v11, v11
	v_mul_f32_e32 v110, 0x3c800000, v110
	v_mul_f32_e32 v111, 0x3c800000, v111
	v_mul_f32_e32 v112, 0x3c800000, v112
	v_mul_f32_e32 v113, 0x3c800000, v113
	v_mul_f32_e32 v102, 0x3c800000, v102
	v_mul_f32_e32 v103, 0x3c800000, v103
	v_mul_f32_e32 v104, 0x3c800000, v104
	v_mul_f32_e32 v105, 0x3c800000, v105
	v_add_f32_e32 v4, 1.0, v4
	v_add_f32_e32 v5, 1.0, v5
	v_add_f32_e32 v6, 1.0, v6
	v_add_f32_e32 v7, 1.0, v7
	v_add_f32_e32 v8, 1.0, v8
	v_add_f32_e32 v9, 1.0, v9
	v_add_f32_e32 v10, 1.0, v10
	v_add_f32_e32 v11, 1.0, v11
	v_rcp_f32_e32 v4, v4
	v_rcp_f32_e32 v5, v5
	v_rcp_f32_e32 v6, v6
	v_rcp_f32_e32 v7, v7
	v_rcp_f32_e32 v8, v8
	v_rcp_f32_e32 v9, v9
	v_rcp_f32_e32 v10, v10
	v_rcp_f32_e32 v11, v11
	v_add_u32_e32 v17, 0x18000, v146
	v_mov_b32_e32 v14, v147
	v_mov_b32_e32 v15, v147
	v_mul_f32_e32 v4, v106, v4
	v_mul_f32_e32 v5, v107, v5
	v_mul_f32_e32 v6, v108, v6
	v_mul_f32_e32 v7, v109, v7
	v_mul_f32_e32 v8, v98, v8
	v_mul_f32_e32 v9, v99, v9
	v_mul_f32_e32 v10, v100, v10
	v_mul_f32_e32 v11, v101, v11
	v_mul_f32_e32 v4, v110, v4
	v_mul_f32_e32 v5, v111, v5
	v_mul_f32_e32 v6, v112, v6
	v_mul_f32_e32 v7, v113, v7
	v_mul_f32_e32 v8, v102, v8
	v_mul_f32_e32 v9, v103, v9
	v_mul_f32_e32 v10, v104, v10
	v_mul_f32_e32 v11, v105, v11
	v_med3_f32 v4, v4, s30, v224
	v_med3_f32 v5, v5, s30, v224
	v_med3_f32 v6, v6, s30, v224
	v_med3_f32 v7, v7, s30, v224
	v_med3_f32 v8, v8, s30, v224
	v_med3_f32 v9, v9, s30, v224
	v_med3_f32 v10, v10, s30, v224
	v_med3_f32 v11, v11, s30, v224
	v_cvt_pk_fp8_f32 v14, v4, v5
	v_cvt_pk_fp8_f32 v14, v6, v7 op_sel:[0,0,1]
	v_cvt_pk_fp8_f32 v15, v8, v9
	v_cvt_pk_fp8_f32 v15, v10, v11 op_sel:[0,0,1]
	global_store_dwordx2 v17, v[14:15], s[16:17]
	v_mul_f32_e32 v90, 0x3c800000, v90
	v_mul_f32_e32 v91, 0x3c800000, v91
	v_mul_f32_e32 v92, 0x3c800000, v92
	v_mul_f32_e32 v93, 0x3c800000, v93
	v_mul_f32_e32 v82, 0x3c800000, v82
	v_mul_f32_e32 v83, 0x3c800000, v83
	v_mul_f32_e32 v84, 0x3c800000, v84
	v_mul_f32_e32 v85, 0x3c800000, v85
	v_mul_f32_e32 v4, 0xbfb8aa3b, v90
	v_mul_f32_e32 v5, 0xbfb8aa3b, v91
	v_mul_f32_e32 v6, 0xbfb8aa3b, v92
	v_mul_f32_e32 v7, 0xbfb8aa3b, v93
	v_mul_f32_e32 v8, 0xbfb8aa3b, v82
	v_mul_f32_e32 v9, 0xbfb8aa3b, v83
	v_mul_f32_e32 v10, 0xbfb8aa3b, v84
	v_mul_f32_e32 v11, 0xbfb8aa3b, v85
	v_exp_f32_e32 v4, v4
	v_exp_f32_e32 v5, v5
	v_exp_f32_e32 v6, v6
; __device__ __forceinline__ float sigmoid_(float x) { return 1.f / (1.f + __expf(-x)); }
; __device__ __forceinline__ float silu_(float x) { return x * sigmoid_(x); }
; __device__ __forceinline__ float sigmoid_fast(float x) { return __builtin_amdgcn_rcpf(1.f + __expf(-x)); }
; __device__ __forceinline__ float silu_fast(float x) { return x * sigmoid_fast(x); }
; __device__ __forceinline__ float one_minus_exp(float x) { const float p = -x * (1.f + x * (0.5f + x * (0.16666667f + x * (0.041666668f + x * 0.0083333338f)))); return x > -0.1f ? p : 1.f - __expf(x); }
; __device__ __forceinline__ float sat8(float x) { return __builtin_amdgcn_fmed3f(x, -448.f, 448.f); }
; __device__ __forceinline__ unsigned pk4_fp8(float a, float b, float c, float d) { int w = __builtin_amdgcn_cvt_pk_fp8_f32(sat8(a), sat8(b), 0, false); w = __builtin_amdgcn_cvt_pk_fp8_f32(sat8(c), sat8(d), w, true); return (unsigned)w; }
;     __device__ __forceinline__ void epi(const f32x4 (&acc)[2][2][4][2], const Unit& u, int wr, int wc, int fr, int fq) const {
;     ...
; #pragma unroll
;         for (int ai = 0; ai < 2; ++ai)
; #pragma unroll
;             for (int m = 0; m < 4; ++m) {
;                 float o[8];
; #pragma unroll
;                 for (int n = 0; n < 2; ++n)
; #pragma unroll
;                     for (int j = 0; j < 4; ++j) o[n * 4 + j] = silu_fast(acc[ai][0][m][n][j] * S) * (acc[ai][1][m][n][j] * S);
;                 u32x2 w; w.x = pk4_fp8(o[0], o[1], o[2], o[3]); w.y = pk4_fp8(o[4], o[5], o[6], o[7]);
;                 *(u32x2*)(base + (size_t)(ai * 128 + m * 16) * 2048 + loff) = w; }
	v_exp_f32_e32 v7, v7
	v_exp_f32_e32 v8, v8
	v_exp_f32_e32 v9, v9
	v_exp_f32_e32 v10, v10
	v_exp_f32_e32 v11, v11
	v_mul_f32_e32 v94, 0x3c800000, v94
	v_mul_f32_e32 v95, 0x3c800000, v95
	v_mul_f32_e32 v96, 0x3c800000, v96
	v_mul_f32_e32 v97, 0x3c800000, v97
	v_mul_f32_e32 v86, 0x3c800000, v86
	v_mul_f32_e32 v87, 0x3c800000, v87
	v_mul_f32_e32 v88, 0x3c800000, v88
	v_mul_f32_e32 v89, 0x3c800000, v89
	v_add_f32_e32 v4, 1.0, v4
	v_add_f32_e32 v5, 1.0, v5
	v_add_f32_e32 v6, 1.0, v6
	v_add_f32_e32 v7, 1.0, v7
	v_add_f32_e32 v8, 1.0, v8
	v_add_f32_e32 v9, 1.0, v9
	v_add_f32_e32 v10, 1.0, v10
	v_add_f32_e32 v11, 1.0, v11
	v_rcp_f32_e32 v4, v4
	v_rcp_f32_e32 v5, v5
	v_rcp_f32_e32 v6, v6
	v_rcp_f32_e32 v7, v7
	v_rcp_f32_e32 v8, v8
	v_rcp_f32_e32 v9, v9
	v_rcp_f32_e32 v10, v10
	v_rcp_f32_e32 v11, v11
	v_add_u32_e32 v16, 0x40000, v146
	v_mov_b32_e32 v12, v147
	v_mov_b32_e32 v13, v147
	v_mul_f32_e32 v4, v90, v4
	v_mul_f32_e32 v5, v91, v5
	v_mul_f32_e32 v6, v92, v6
	v_mul_f32_e32 v7, v93, v7
	v_mul_f32_e32 v8, v82, v8
	v_mul_f32_e32 v9, v83, v9
	v_mul_f32_e32 v10, v84, v10
	v_mul_f32_e32 v11, v85, v11
	v_mul_f32_e32 v4, v94, v4
	v_mul_f32_e32 v5, v95, v5
	v_mul_f32_e32 v6, v96, v6
	v_mul_f32_e32 v7, v97, v7
	v_mul_f32_e32 v8, v86, v8
	v_mul_f32_e32 v9, v87, v9
	v_mul_f32_e32 v10, v88, v10
	v_mul_f32_e32 v11, v89, v11
	v_med3_f32 v4, v4, s30, v224
	v_med3_f32 v5, v5, s30, v224
	v_med3_f32 v6, v6, s30, v224
	v_med3_f32 v7, v7, s30, v224
	v_med3_f32 v8, v8, s30, v224
	v_med3_f32 v9, v9, s30, v224
	v_med3_f32 v10, v10, s30, v224
	v_med3_f32 v11, v11, s30, v224
	v_cvt_pk_fp8_f32 v12, v4, v5
	v_cvt_pk_fp8_f32 v12, v6, v7 op_sel:[0,0,1]
	v_cvt_pk_fp8_f32 v13, v8, v9
	v_cvt_pk_fp8_f32 v13, v10, v11 op_sel:[0,0,1]
	global_store_dwordx2 v16, v[12:13], s[16:17]
	v_mul_f32_e32 v74, 0x3c800000, v74
	v_mul_f32_e32 v75, 0x3c800000, v75
	v_mul_f32_e32 v76, 0x3c800000, v76
	v_mul_f32_e32 v77, 0x3c800000, v77
	v_mul_f32_e32 v66, 0x3c800000, v66
	v_mul_f32_e32 v67, 0x3c800000, v67
	v_mul_f32_e32 v68, 0x3c800000, v68
	v_mul_f32_e32 v69, 0x3c800000, v69
	v_mul_f32_e32 v4, 0xbfb8aa3b, v74
	v_mul_f32_e32 v5, 0xbfb8aa3b, v75
	v_mul_f32_e32 v6, 0xbfb8aa3b, v76
	v_mul_f32_e32 v7, 0xbfb8aa3b, v77
	v_mul_f32_e32 v8, 0xbfb8aa3b, v66
	v_mul_f32_e32 v9, 0xbfb8aa3b, v67
	v_mul_f32_e32 v10, 0xbfb8aa3b, v68
	v_mul_f32_e32 v11, 0xbfb8aa3b, v69
	v_exp_f32_e32 v4, v4
	v_exp_f32_e32 v5, v5
	v_exp_f32_e32 v6, v6
	v_exp_f32_e32 v7, v7
	v_exp_f32_e32 v8, v8
	v_exp_f32_e32 v9, v9
	v_exp_f32_e32 v10, v10
	v_exp_f32_e32 v11, v11
	v_mul_f32_e32 v78, 0x3c800000, v78
	v_mul_f32_e32 v79, 0x3c800000, v79
	v_mul_f32_e32 v80, 0x3c800000, v80
	v_mul_f32_e32 v81, 0x3c800000, v81
	v_mul_f32_e32 v70, 0x3c800000, v70
	v_mul_f32_e32 v71, 0x3c800000, v71
	v_mul_f32_e32 v72, 0x3c800000, v72
	v_mul_f32_e32 v73, 0x3c800000, v73
	v_add_f32_e32 v4, 1.0, v4
	v_add_f32_e32 v5, 1.0, v5
	v_add_f32_e32 v6, 1.0, v6
	v_add_f32_e32 v7, 1.0, v7
	v_add_f32_e32 v8, 1.0, v8
	v_add_f32_e32 v9, 1.0, v9
	v_add_f32_e32 v10, 1.0, v10
	v_add_f32_e32 v11, 1.0, v11
	v_rcp_f32_e32 v4, v4
	v_rcp_f32_e32 v5, v5
	v_rcp_f32_e32 v6, v6
	v_rcp_f32_e32 v7, v7
	v_rcp_f32_e32 v8, v8
	v_rcp_f32_e32 v9, v9
	v_rcp_f32_e32 v10, v10
	v_rcp_f32_e32 v11, v11
	v_add_u32_e32 v17, 0x48000, v146
	v_mov_b32_e32 v14, v147
	v_mov_b32_e32 v15, v147
	v_mul_f32_e32 v4, v74, v4
	v_mul_f32_e32 v5, v75, v5
	v_mul_f32_e32 v6, v76, v6
	v_mul_f32_e32 v7, v77, v7
	v_mul_f32_e32 v8, v66, v8
	v_mul_f32_e32 v9, v67, v9
	v_mul_f32_e32 v10, v68, v10
	v_mul_f32_e32 v11, v69, v11
	v_mul_f32_e32 v4, v78, v4
	v_mul_f32_e32 v5, v79, v5
	v_mul_f32_e32 v6, v80, v6
	v_mul_f32_e32 v7, v81, v7
	v_mul_f32_e32 v8, v70, v8
	v_mul_f32_e32 v9, v71, v9
	v_mul_f32_e32 v10, v72, v10
	v_mul_f32_e32 v11, v73, v11
	v_med3_f32 v4, v4, s30, v224
	v_med3_f32 v5, v5, s30, v224
	v_med3_f32 v6, v6, s30, v224
	v_med3_f32 v7, v7, s30, v224
	v_med3_f32 v8, v8, s30, v224
	v_med3_f32 v9, v9, s30, v224
	v_med3_f32 v10, v10, s30, v224
	v_med3_f32 v11, v11, s30, v224
	v_cvt_pk_fp8_f32 v14, v4, v5
	v_cvt_pk_fp8_f32 v14, v6, v7 op_sel:[0,0,1]
	v_cvt_pk_fp8_f32 v15, v8, v9
	v_cvt_pk_fp8_f32 v15, v10, v11 op_sel:[0,0,1]
	global_store_dwordx2 v17, v[14:15], s[16:17]
	v_mul_f32_e32 v58, 0x3c800000, v58
	v_mul_f32_e32 v59, 0x3c800000, v59
	v_mul_f32_e32 v60, 0x3c800000, v60
	v_mul_f32_e32 v61, 0x3c800000, v61
	v_mul_f32_e32 v50, 0x3c800000, v50
	v_mul_f32_e32 v51, 0x3c800000, v51
	v_mul_f32_e32 v52, 0x3c800000, v52
	v_mul_f32_e32 v53, 0x3c800000, v53
	v_mul_f32_e32 v4, 0xbfb8aa3b, v58
	v_mul_f32_e32 v5, 0xbfb8aa3b, v59
	v_mul_f32_e32 v6, 0xbfb8aa3b, v60
	v_mul_f32_e32 v7, 0xbfb8aa3b, v61
; __device__ __forceinline__ float silu_fast(float x) { return x * sigmoid_fast(x); }
; __device__ __forceinline__ unsigned pk4_fp8(float a, float b, float c, float d) { int w = __builtin_amdgcn_cvt_pk_fp8_f32(sat8(a), sat8(b), 0, false); w = __builtin_amdgcn_cvt_pk_fp8_f32(sat8(c), sat8(d), w, true); return (unsigned)w; }
;     __device__ __forceinline__ void epi(const f32x4 (&acc)[2][2][4][2], const Unit& u, int wr, int wc, int fr, int fq) const {
;         const int e = u.pm / tpe, t = u.pm - e * tpe;
;         char* base = (char*)(ACT + ((size_t)e * EROWS + (size_t)t * 256) * 2048 + (size_t)u.pn * 128);
;     ...
; #pragma unroll
;         for (int ai = 0; ai < 2; ++ai)
; #pragma unroll
;             for (int m = 0; m < 4; ++m) {
;                 float o[8];
; #pragma unroll
;                 for (int n = 0; n < 2; ++n)
; #pragma unroll
;                     for (int j = 0; j < 4; ++j) o[n * 4 + j] = silu_fast(acc[ai][0][m][n][j] * S) * (acc[ai][1][m][n][j] * S);
;                 u32x2 w; w.x = pk4_fp8(o[0], o[1], o[2], o[3]); w.y = pk4_fp8(o[4], o[5], o[6], o[7]);
;                 *(u32x2*)(base + (size_t)(ai * 128 + m * 16) * 2048 + loff) = w; }
	v_mul_f32_e32 v8, 0xbfb8aa3b, v50
	v_mul_f32_e32 v9, 0xbfb8aa3b, v51
	v_mul_f32_e32 v10, 0xbfb8aa3b, v52
	v_mul_f32_e32 v11, 0xbfb8aa3b, v53
	v_exp_f32_e32 v4, v4
	v_exp_f32_e32 v5, v5
	v_exp_f32_e32 v6, v6
	v_exp_f32_e32 v7, v7
	v_exp_f32_e32 v8, v8
	v_exp_f32_e32 v9, v9
	v_exp_f32_e32 v10, v10
	v_exp_f32_e32 v11, v11
	v_mul_f32_e32 v62, 0x3c800000, v62
	v_mul_f32_e32 v63, 0x3c800000, v63
	v_mul_f32_e32 v64, 0x3c800000, v64
	v_mul_f32_e32 v65, 0x3c800000, v65
	v_mul_f32_e32 v54, 0x3c800000, v54
	v_mul_f32_e32 v55, 0x3c800000, v55
	v_mul_f32_e32 v56, 0x3c800000, v56
	v_mul_f32_e32 v57, 0x3c800000, v57
	v_add_f32_e32 v4, 1.0, v4
	v_add_f32_e32 v5, 1.0, v5
	v_add_f32_e32 v6, 1.0, v6
	v_add_f32_e32 v7, 1.0, v7
	v_add_f32_e32 v8, 1.0, v8
	v_add_f32_e32 v9, 1.0, v9
	v_add_f32_e32 v10, 1.0, v10
	v_add_f32_e32 v11, 1.0, v11
	v_rcp_f32_e32 v4, v4
	v_rcp_f32_e32 v5, v5
	v_rcp_f32_e32 v6, v6
	v_rcp_f32_e32 v7, v7
	v_rcp_f32_e32 v8, v8
	v_rcp_f32_e32 v9, v9
	v_rcp_f32_e32 v10, v10
	v_rcp_f32_e32 v11, v11
	v_add_u32_e32 v16, 0x50000, v146
	v_mov_b32_e32 v12, v147
	v_mov_b32_e32 v13, v147
	v_mul_f32_e32 v4, v58, v4
	v_mul_f32_e32 v5, v59, v5
	v_mul_f32_e32 v6, v60, v6
	v_mul_f32_e32 v7, v61, v7
	v_mul_f32_e32 v8, v50, v8
	v_mul_f32_e32 v9, v51, v9
	v_mul_f32_e32 v10, v52, v10
	v_mul_f32_e32 v11, v53, v11
	v_mul_f32_e32 v4, v62, v4
	v_mul_f32_e32 v5, v63, v5
	v_mul_f32_e32 v6, v64, v6
	v_mul_f32_e32 v7, v65, v7
	v_mul_f32_e32 v8, v54, v8
	v_mul_f32_e32 v9, v55, v9
	v_mul_f32_e32 v10, v56, v10
	v_mul_f32_e32 v11, v57, v11
	v_med3_f32 v4, v4, s30, v224
	v_med3_f32 v5, v5, s30, v224
	v_med3_f32 v6, v6, s30, v224
	v_med3_f32 v7, v7, s30, v224
	v_med3_f32 v8, v8, s30, v224
	v_med3_f32 v9, v9, s30, v224
	v_med3_f32 v10, v10, s30, v224
	v_med3_f32 v11, v11, s30, v224
	v_cvt_pk_fp8_f32 v12, v4, v5
	v_cvt_pk_fp8_f32 v12, v6, v7 op_sel:[0,0,1]
	v_cvt_pk_fp8_f32 v13, v8, v9
	v_cvt_pk_fp8_f32 v13, v10, v11 op_sel:[0,0,1]
	global_store_dwordx2 v16, v[12:13], s[16:17]
	v_mul_f32_e32 v42, 0x3c800000, v42
	v_mul_f32_e32 v43, 0x3c800000, v43
	v_mul_f32_e32 v44, 0x3c800000, v44
	v_mul_f32_e32 v45, 0x3c800000, v45
	v_mul_f32_e32 v38, 0x3c800000, v38
	v_mul_f32_e32 v39, 0x3c800000, v39
	v_mul_f32_e32 v40, 0x3c800000, v40
	v_mul_f32_e32 v41, 0x3c800000, v41
	v_mul_f32_e32 v4, 0xbfb8aa3b, v42
	v_mul_f32_e32 v5, 0xbfb8aa3b, v43
	v_mul_f32_e32 v6, 0xbfb8aa3b, v44
	v_mul_f32_e32 v7, 0xbfb8aa3b, v45
	v_mul_f32_e32 v8, 0xbfb8aa3b, v38
	v_mul_f32_e32 v9, 0xbfb8aa3b, v39
	v_mul_f32_e32 v10, 0xbfb8aa3b, v40
	v_mul_f32_e32 v11, 0xbfb8aa3b, v41
	v_exp_f32_e32 v4, v4
	v_exp_f32_e32 v5, v5
	v_exp_f32_e32 v6, v6
	v_exp_f32_e32 v7, v7
	v_exp_f32_e32 v8, v8
	v_exp_f32_e32 v9, v9
	v_exp_f32_e32 v10, v10
	v_exp_f32_e32 v11, v11
	v_mul_f32_e32 v46, 0x3c800000, v46
	v_mul_f32_e32 v47, 0x3c800000, v47
	v_mul_f32_e32 v48, 0x3c800000, v48
	v_mul_f32_e32 v49, 0x3c800000, v49
	v_mul_f32_e32 v34, 0x3c800000, v34
	v_mul_f32_e32 v35, 0x3c800000, v35
	v_mul_f32_e32 v36, 0x3c800000, v36
	v_mul_f32_e32 v37, 0x3c800000, v37
	v_add_f32_e32 v4, 1.0, v4
	v_add_f32_e32 v5, 1.0, v5
	v_add_f32_e32 v6, 1.0, v6
	v_add_f32_e32 v7, 1.0, v7
	v_add_f32_e32 v8, 1.0, v8
	v_add_f32_e32 v9, 1.0, v9
	v_add_f32_e32 v10, 1.0, v10
	v_add_f32_e32 v11, 1.0, v11
	v_rcp_f32_e32 v4, v4
	v_rcp_f32_e32 v5, v5
	v_rcp_f32_e32 v6, v6
	v_rcp_f32_e32 v7, v7
	v_rcp_f32_e32 v8, v8
	v_rcp_f32_e32 v9, v9
	v_rcp_f32_e32 v10, v10
	v_rcp_f32_e32 v11, v11
	v_add_u32_e32 v17, 0x58000, v146
	v_mov_b32_e32 v14, v147
	v_mov_b32_e32 v15, v147
	v_mul_f32_e32 v4, v42, v4
	v_mul_f32_e32 v5, v43, v5
	v_mul_f32_e32 v6, v44, v6
	v_mul_f32_e32 v7, v45, v7
	v_mul_f32_e32 v8, v38, v8
	v_mul_f32_e32 v9, v39, v9
	v_mul_f32_e32 v10, v40, v10
	v_mul_f32_e32 v11, v41, v11
	v_mul_f32_e32 v4, v46, v4
	v_mul_f32_e32 v5, v47, v5
	v_mul_f32_e32 v6, v48, v6
	v_mul_f32_e32 v7, v49, v7
	v_mul_f32_e32 v8, v34, v8
	v_mul_f32_e32 v9, v35, v9
	v_mul_f32_e32 v10, v36, v10
	v_mul_f32_e32 v11, v37, v11
	v_med3_f32 v4, v4, s30, v224
	v_med3_f32 v5, v5, s30, v224
	v_med3_f32 v6, v6, s30, v224
	v_med3_f32 v7, v7, s30, v224
	v_med3_f32 v8, v8, s30, v224
	v_med3_f32 v9, v9, s30, v224
	v_med3_f32 v10, v10, s30, v224
	v_med3_f32 v11, v11, s30, v224
	v_cvt_pk_fp8_f32 v14, v4, v5
	v_cvt_pk_fp8_f32 v14, v6, v7 op_sel:[0,0,1]
	v_cvt_pk_fp8_f32 v15, v8, v9
	v_cvt_pk_fp8_f32 v15, v10, v11 op_sel:[0,0,1]
	global_store_dwordx2 v17, v[14:15], s[16:17]
	s_mov_b64 s[16:17], -1
	s_mov_b32 s18, 0x3c800000
	s_mov_b32 s11, 0x50000
	s_and_b64 vcc, exec, s[38:39]
	s_cbranch_vccnz .LBB0_2580
	s_andn2_b64 vcc, exec, s[4:5]
	s_cbranch_vccnz .LBB0_2579
	s_barrier
	s_branch .LBB0_2579
